# hand-written GEMM+epilogue tail for both gcn kernels: bias through MFMA SrcC tuple, cvt_pk_f16 + ds_write_b16/_d16_hi, saddr row stores
# speedup vs baseline: 1.0085x; 1.0060x over previous
.LBB4_29:
	s_or_b64 exec, exec, s[4:5]
	s_waitcnt lgkmcnt(1)
	v_fma_mixlo_f16 v11, v14, v2, 0
	v_mov_b32_e32 v2, v3
	v_mov_b32_e32 v3, v4
	v_mov_b32_e32 v4, v5
	v_mov_b32_e32 v5, v6
	v_pk_mul_f32 v[4:5], v[14:15], v[4:5] op_sel_hi:[0,1]
	v_cvt_pk_f16_f32 v6, v4, v5
	v_mov_b32_e32 v4, v7
	v_mov_b32_e32 v5, v8
	v_pk_mul_f32 v[4:5], v[14:15], v[4:5] op_sel_hi:[0,1]
	v_pk_mul_f32 v[2:3], v[14:15], v[2:3] op_sel_hi:[0,1]
	v_cvt_pk_f16_f32 v5, v4, v5
	v_cvt_pk_f16_f32 v3, v2, v3
	v_alignbit_b32 v4, v5, v6, 16
	v_lshrrev_b32_e32 v5, 16, v5
	s_movk_i32 s0, 0x50
	v_pack_b32_f16 v2, v11, v3
	v_alignbit_b32 v3, v6, v3, 16
	v_fma_mixhi_f16 v5, v14, v9, 0
	v_mad_u32_u24 v6, v19, s0, v35
	ds_write_b128 v6, v[2:5]
	v_lshlrev_b32_e32 v2, 4, v0
	v_lshrrev_b32_e32 v35, 2, v0
	v_and_b32_e32 v18, 48, v2
	v_mad_u32_u24 v2, v35, s0, v18
	s_waitcnt lgkmcnt(0)
	s_barrier
	ds_read_b128 v[2:5], v2
	v_add_u32_e32 v6, s3, v35
	v_ashrrev_i32_e32 v7, 31, v6
	v_lshlrev_b64 v[6:7], 6, v[6:7]
	v_lshl_add_u64 v[6:7], s[18:19], 0, v[6:7]
	v_mov_b32_e32 v19, 0
	v_lshl_add_u64 v[6:7], v[6:7], 0, v[18:19]
	s_waitcnt lgkmcnt(0)
	global_store_dwordx4 v[6:7], v[2:5], off nt
	s_nop 1
	v_and_b32_e32 v4, 15, v0
	v_bfe_u32 v5, v0, 4, 2
	v_lshrrev_b32_e32 v6, 6, v0
	v_and_b32_e32 v7, 63, v0
	v_lshlrev_b32_e32 v1, 11, v6
	v_lshl_add_u32 v1, v7, 4, v1
	v_lshl_or_b32 v7, v6, 5, v4
	v_lshlrev_b32_e32 v2, 2, v7
	global_load_dword v40, v2, s[10:11]
	global_load_dword v44, v2, s[10:11] offset:64
	global_load_dwordx4 v[48:51], v1, s[8:9] offset:0
	global_load_dwordx4 v[52:55], v1, s[8:9] offset:1024
	s_movk_i32 s20, 0x50
	v_mul_u32_u24_e32 v2, s20, v4
	v_lshl_add_u32 v2, v5, 4, v2
	v_mul_u32_u24_e32 v3, 0x440, v5
	v_lshl_add_u32 v3, v7, 1, v3
	ds_read_b128 v[56:59], v2 offset:0
	ds_read_b128 v[60:63], v2 offset:1280
	ds_read_b128 v[64:67], v2 offset:2560
	ds_read_b128 v[68:71], v2 offset:3840
	s_waitcnt vmcnt(2)
	v_mov_b32_e32 v41, v40
	v_mov_b32_e32 v42, v40
	v_mov_b32_e32 v43, v40
	v_mov_b32_e32 v45, v44
	v_mov_b32_e32 v46, v44
	v_mov_b32_e32 v47, v44
	s_waitcnt vmcnt(0)
	s_waitcnt lgkmcnt(0)
	v_mfma_f32_16x16x32_f16 v[8:11], v[56:59], v[48:51], v[40:43]
	v_mfma_f32_16x16x32_f16 v[16:19], v[60:63], v[48:51], v[40:43]
	v_mfma_f32_16x16x32_f16 v[24:27], v[64:67], v[48:51], v[40:43]
	v_mfma_f32_16x16x32_f16 v[32:35], v[68:71], v[48:51], v[40:43]
	v_mfma_f32_16x16x32_f16 v[12:15], v[56:59], v[52:55], v[44:47]
	v_mfma_f32_16x16x32_f16 v[20:23], v[60:63], v[52:55], v[44:47]
	v_mfma_f32_16x16x32_f16 v[28:31], v[64:67], v[52:55], v[44:47]
	v_mfma_f32_16x16x32_f16 v[36:39], v[68:71], v[52:55], v[44:47]
	s_barrier
	v_and_b32_e32 v40, 63, v0
	v_xor_b32_e32 v41, 32, v40
	v_xor_b32_e32 v40, 16, v40
	v_lshlrev_b32_e32 v40, 2, v40
	v_lshlrev_b32_e32 v41, 2, v41
	s_nop 3
	v_max_f32_e32 v8, 0, v8
	v_max_f32_e32 v9, 0, v9
	v_max_f32_e32 v10, 0, v10
	v_max_f32_e32 v11, 0, v11
	v_mov_b32_e32 v1, v8
	v_mul_f32_e32 v2, v8, v8
	v_add_f32_e32 v1, v1, v9
	v_fmac_f32_e32 v2, v9, v9
	v_add_f32_e32 v1, v1, v10
	v_fmac_f32_e32 v2, v10, v10
	v_add_f32_e32 v1, v1, v11
	v_fmac_f32_e32 v2, v11, v11
	v_cvt_pk_f16_f32 v8, v8, v9
	ds_write_b16 v3, v8 offset:0
	ds_write_b16_d16_hi v3, v8 offset:272
	v_cvt_pk_f16_f32 v10, v10, v11
	ds_write_b16 v3, v10 offset:544
	ds_write_b16_d16_hi v3, v10 offset:816
	v_max_f32_e32 v16, 0, v16
	v_max_f32_e32 v17, 0, v17
	v_max_f32_e32 v18, 0, v18
	v_max_f32_e32 v19, 0, v19
	v_add_f32_e32 v1, v1, v16
	v_fmac_f32_e32 v2, v16, v16
	v_add_f32_e32 v1, v1, v17
	v_fmac_f32_e32 v2, v17, v17
	v_add_f32_e32 v1, v1, v18
	v_fmac_f32_e32 v2, v18, v18
	v_add_f32_e32 v1, v1, v19
	v_fmac_f32_e32 v2, v19, v19
	v_cvt_pk_f16_f32 v16, v16, v17
	ds_write_b16 v3, v16 offset:4352
	ds_write_b16_d16_hi v3, v16 offset:4624
	v_cvt_pk_f16_f32 v18, v18, v19
	ds_write_b16 v3, v18 offset:4896
	ds_write_b16_d16_hi v3, v18 offset:5168
	v_max_f32_e32 v24, 0, v24
	v_max_f32_e32 v25, 0, v25
	v_max_f32_e32 v26, 0, v26
	v_max_f32_e32 v27, 0, v27
	v_add_f32_e32 v1, v1, v24
	v_fmac_f32_e32 v2, v24, v24
	v_add_f32_e32 v1, v1, v25
	v_fmac_f32_e32 v2, v25, v25
	v_add_f32_e32 v1, v1, v26
	v_fmac_f32_e32 v2, v26, v26
	v_add_f32_e32 v1, v1, v27
	v_fmac_f32_e32 v2, v27, v27
	v_cvt_pk_f16_f32 v24, v24, v25
	ds_write_b16 v3, v24 offset:8704
	ds_write_b16_d16_hi v3, v24 offset:8976
	v_cvt_pk_f16_f32 v26, v26, v27
	ds_write_b16 v3, v26 offset:9248
	ds_write_b16_d16_hi v3, v26 offset:9520
	v_max_f32_e32 v32, 0, v32
	v_max_f32_e32 v33, 0, v33
	v_max_f32_e32 v34, 0, v34
	v_max_f32_e32 v35, 0, v35
	v_add_f32_e32 v1, v1, v32
	v_fmac_f32_e32 v2, v32, v32
	v_add_f32_e32 v1, v1, v33
	v_fmac_f32_e32 v2, v33, v33
	v_add_f32_e32 v1, v1, v34
	v_fmac_f32_e32 v2, v34, v34
	v_add_f32_e32 v1, v1, v35
	v_fmac_f32_e32 v2, v35, v35
	v_cvt_pk_f16_f32 v32, v32, v33
	ds_write_b16 v3, v32 offset:13056
	ds_write_b16_d16_hi v3, v32 offset:13328
	v_cvt_pk_f16_f32 v34, v34, v35
	ds_write_b16 v3, v34 offset:13600
	ds_write_b16_d16_hi v3, v34 offset:13872
	v_max_f32_e32 v12, 0, v12
	v_max_f32_e32 v13, 0, v13
	v_max_f32_e32 v14, 0, v14
	v_max_f32_e32 v15, 0, v15
	v_mov_b32_e32 v4, v12
	v_mul_f32_e32 v5, v12, v12
	v_add_f32_e32 v4, v4, v13
	v_fmac_f32_e32 v5, v13, v13
	v_add_f32_e32 v4, v4, v14
	v_fmac_f32_e32 v5, v14, v14
	v_add_f32_e32 v4, v4, v15
	v_fmac_f32_e32 v5, v15, v15
	v_cvt_pk_f16_f32 v12, v12, v13
	ds_write_b16 v3, v12 offset:32
	ds_write_b16_d16_hi v3, v12 offset:304
	v_cvt_pk_f16_f32 v14, v14, v15
	ds_write_b16 v3, v14 offset:576
	ds_write_b16_d16_hi v3, v14 offset:848
	v_max_f32_e32 v20, 0, v20
	v_max_f32_e32 v21, 0, v21
	v_max_f32_e32 v22, 0, v22
	v_max_f32_e32 v23, 0, v23
	v_add_f32_e32 v4, v4, v20
	v_fmac_f32_e32 v5, v20, v20
	v_add_f32_e32 v4, v4, v21
	v_fmac_f32_e32 v5, v21, v21
	v_add_f32_e32 v4, v4, v22
	v_fmac_f32_e32 v5, v22, v22
	v_add_f32_e32 v4, v4, v23
	v_fmac_f32_e32 v5, v23, v23
	v_cvt_pk_f16_f32 v20, v20, v21
	ds_write_b16 v3, v20 offset:4384
	ds_write_b16_d16_hi v3, v20 offset:4656
	v_cvt_pk_f16_f32 v22, v22, v23
	ds_write_b16 v3, v22 offset:4928
	ds_write_b16_d16_hi v3, v22 offset:5200
	v_max_f32_e32 v28, 0, v28
	v_max_f32_e32 v29, 0, v29
	v_max_f32_e32 v30, 0, v30
	v_max_f32_e32 v31, 0, v31
	v_add_f32_e32 v4, v4, v28
	v_fmac_f32_e32 v5, v28, v28
	v_add_f32_e32 v4, v4, v29
	v_fmac_f32_e32 v5, v29, v29
	v_add_f32_e32 v4, v4, v30
	v_fmac_f32_e32 v5, v30, v30
	v_add_f32_e32 v4, v4, v31
	v_fmac_f32_e32 v5, v31, v31
	v_cvt_pk_f16_f32 v28, v28, v29
	ds_write_b16 v3, v28 offset:8736
	ds_write_b16_d16_hi v3, v28 offset:9008
	v_cvt_pk_f16_f32 v30, v30, v31
	ds_write_b16 v3, v30 offset:9280
	ds_write_b16_d16_hi v3, v30 offset:9552
	v_max_f32_e32 v36, 0, v36
	v_max_f32_e32 v37, 0, v37
	v_max_f32_e32 v38, 0, v38
	v_max_f32_e32 v39, 0, v39
	v_add_f32_e32 v4, v4, v36
	v_fmac_f32_e32 v5, v36, v36
	v_add_f32_e32 v4, v4, v37
	v_fmac_f32_e32 v5, v37, v37
	v_add_f32_e32 v4, v4, v38
	v_fmac_f32_e32 v5, v38, v38
	v_add_f32_e32 v4, v4, v39
	v_fmac_f32_e32 v5, v39, v39
	v_cvt_pk_f16_f32 v36, v36, v37
	ds_write_b16 v3, v36 offset:13088
	ds_write_b16_d16_hi v3, v36 offset:13360
	v_cvt_pk_f16_f32 v38, v38, v39
	ds_write_b16 v3, v38 offset:13632
	ds_write_b16_d16_hi v3, v38 offset:13904
	ds_bpermute_b32 v9, v40, v1
	ds_bpermute_b32 v11, v40, v2
	ds_bpermute_b32 v13, v40, v4
	ds_bpermute_b32 v15, v40, v5
	s_waitcnt lgkmcnt(0)
	v_add_f32_e32 v1, v1, v9
	v_add_f32_e32 v2, v2, v11
	v_add_f32_e32 v4, v4, v13
	v_add_f32_e32 v5, v5, v15
	ds_bpermute_b32 v9, v41, v1
	ds_bpermute_b32 v11, v41, v2
	ds_bpermute_b32 v13, v41, v4
	ds_bpermute_b32 v15, v41, v5
	s_waitcnt lgkmcnt(0)
	v_add_f32_e32 v1, v1, v9
	v_add_f32_e32 v2, v2, v11
	v_add_f32_e32 v4, v4, v13
	v_add_f32_e32 v5, v5, v15
	v_and_b32_e32 v6, 63, v0
	v_cmp_gt_u32_e32 vcc, 16, v6
	v_lshlrev_b32_e32 v6, 2, v7
	s_and_saveexec_b64 s[22:23], vcc
	ds_write_b32 v6, v1 offset:17408
	ds_write_b32 v6, v2 offset:17920
	ds_write_b32 v6, v4 offset:17472
	ds_write_b32 v6, v5 offset:17984
	s_or_b64 exec, exec, s[22:23]
	s_waitcnt lgkmcnt(0)
	s_barrier
	v_lshrrev_b32_e32 v6, 4, v0
	v_mul_u32_u24_e32 v6, 0x110, v6
	v_and_b32_e32 v40, 15, v0
	v_lshl_add_u32 v6, v40, 4, v6
	ds_read_b128 v[16:19], v6 offset:0
	ds_read_b128 v[20:23], v6 offset:4352
	ds_read_b128 v[24:27], v6 offset:8704
	ds_read_b128 v[28:31], v6 offset:13056
	v_lshlrev_b32_e32 v41, 2, v0
	ds_read_b32 v1, v41 offset:17408
	s_lshl_b32 s20, s3, 8
	s_add_u32 s24, s14, s20
	s_addc_u32 s25, s15, 0
	v_lshlrev_b32_e32 v40, 4, v0
	s_waitcnt lgkmcnt(4)
	global_store_dwordx4 v40, v[16:19], s[24:25] nt
	v_add_u32_e32 v40, 0x1000, v40
	s_waitcnt lgkmcnt(3)
	global_store_dwordx4 v40, v[20:23], s[24:25] nt
	v_add_u32_e32 v40, 0x1000, v40
	s_waitcnt lgkmcnt(2)
	global_store_dwordx4 v40, v[24:27], s[24:25] nt
	v_add_u32_e32 v40, 0x1000, v40
	s_waitcnt lgkmcnt(1)
	global_store_dwordx4 v40, v[28:31], s[24:25] nt
	s_lshl_b32 s20, s2, 8
	s_and_b32 s20, s20, 0xf00
	v_add_lshl_u32 v41, s20, v0, 2
	s_waitcnt lgkmcnt(0)
	global_atomic_add_f32 v41, v1, s[12:13]
	s_endpgm

	.amdhsa_kernel _Z5k_gcnILi1EEvPKvPK15HIP_vector_typeIiLj2EEPfPKiS8_PKfPKDF16_SA_SA_SA_SA_S6_PDF16_S6_SD_SC_SA_
		.amdhsa_group_segment_fixed_size 22272
		.amdhsa_private_segment_fixed_size 0
		.amdhsa_kernarg_size 136
		.amdhsa_user_sgpr_count 2
		.amdhsa_user_sgpr_dispatch_ptr 0
		.amdhsa_user_sgpr_queue_ptr 0
		.amdhsa_user_sgpr_kernarg_segment_ptr 1
		.amdhsa_user_sgpr_dispatch_id 0
		.amdhsa_user_sgpr_kernarg_preload_length 0
		.amdhsa_user_sgpr_kernarg_preload_offset 0
		.amdhsa_user_sgpr_private_segment_size 0
		.amdhsa_uses_dynamic_stack 0
		.amdhsa_enable_private_segment 0
		.amdhsa_system_sgpr_workgroup_id_x 1
		.amdhsa_system_sgpr_workgroup_id_y 0
		.amdhsa_system_sgpr_workgroup_id_z 0
		.amdhsa_system_sgpr_workgroup_info 0
		.amdhsa_system_vgpr_workitem_id 0
		.amdhsa_next_free_vgpr 72
		.amdhsa_next_free_sgpr 75
		.amdhsa_accum_offset 72
		.amdhsa_reserve_vcc 1
		.amdhsa_float_round_mode_32 0
		.amdhsa_float_round_mode_16_64 0
		.amdhsa_float_denorm_mode_32 3
		.amdhsa_float_denorm_mode_16_64 3
		.amdhsa_dx10_clamp 1
		.amdhsa_ieee_mode 1
		.amdhsa_fp16_overflow 0
		.amdhsa_tg_split 0
		.amdhsa_exception_fp_ieee_invalid_op 0
		.amdhsa_exception_fp_denorm_src 0
		.amdhsa_exception_fp_ieee_div_zero 0
		.amdhsa_exception_fp_ieee_overflow 0
		.amdhsa_exception_fp_ieee_underflow 0
		.amdhsa_exception_fp_ieee_inexact 0
		.amdhsa_exception_int_div_zero 0
	.end_amdhsa_kernel

.LBB5_68:
	s_waitcnt vmcnt(0) lgkmcnt(0)
	s_barrier
	v_mov_b32_e32 v1, v78
	v_and_b32_e32 v5, 15, v1
	v_bfe_u32 v6, v1, 4, 2
	v_lshrrev_b32_e32 v7, 6, v1
	v_and_b32_e32 v8, 63, v1
	v_lshlrev_b32_e32 v2, 11, v7
	v_lshl_add_u32 v2, v8, 4, v2
	v_lshl_or_b32 v8, v7, 5, v5
	v_lshlrev_b32_e32 v3, 2, v8
	global_load_dword v42, v3, s[18:19]
	global_load_dword v46, v3, s[18:19] offset:64
	global_load_dwordx4 v[50:53], v2, s[16:17] offset:0
	global_load_dwordx4 v[54:57], v2, s[16:17] offset:1024
	v_add_u32_e32 v2, 0x2000, v2
	global_load_dwordx4 v[58:61], v2, s[16:17] offset:0
	global_load_dwordx4 v[62:65], v2, s[16:17] offset:1024
	v_add_u32_e32 v2, 0x2000, v2
	global_load_dwordx4 v[66:69], v2, s[16:17] offset:0
	global_load_dwordx4 v[70:73], v2, s[16:17] offset:1024
	v_add_u32_e32 v2, 0x2000, v2
	global_load_dwordx4 v[74:77], v2, s[16:17] offset:0
	global_load_dwordx4 v[78:81], v2, s[16:17] offset:1024
	s_movk_i32 s40, 0x110
	v_mul_u32_u24_e32 v3, s40, v5
	v_lshl_add_u32 v3, v6, 4, v3
	v_mul_u32_u24_e32 v4, 0x440, v6
	v_lshl_add_u32 v4, v8, 1, v4
	ds_read_b128 v[82:85], v3 offset:0
	ds_read_b128 v[86:89], v3 offset:4352
	ds_read_b128 v[90:93], v3 offset:8704
	ds_read_b128 v[94:97], v3 offset:13056
	s_waitcnt vmcnt(8)
	v_mov_b32_e32 v43, v42
	v_mov_b32_e32 v44, v42
	v_mov_b32_e32 v45, v42
	v_mov_b32_e32 v47, v46
	v_mov_b32_e32 v48, v46
	v_mov_b32_e32 v49, v46
	ds_read_b128 v[98:101], v3 offset:64
	ds_read_b128 v[102:105], v3 offset:4416
	ds_read_b128 v[106:109], v3 offset:8768
	ds_read_b128 v[110:113], v3 offset:13120
	s_waitcnt vmcnt(6)
	s_waitcnt lgkmcnt(4)
	v_mfma_f32_16x16x32_f16 v[10:13], v[82:85], v[50:53], v[42:45]
	v_mfma_f32_16x16x32_f16 v[18:21], v[86:89], v[50:53], v[42:45]
	v_mfma_f32_16x16x32_f16 v[26:29], v[90:93], v[50:53], v[42:45]
	v_mfma_f32_16x16x32_f16 v[34:37], v[94:97], v[50:53], v[42:45]
	v_mfma_f32_16x16x32_f16 v[14:17], v[82:85], v[54:57], v[46:49]
	v_mfma_f32_16x16x32_f16 v[22:25], v[86:89], v[54:57], v[46:49]
	v_mfma_f32_16x16x32_f16 v[30:33], v[90:93], v[54:57], v[46:49]
	v_mfma_f32_16x16x32_f16 v[38:41], v[94:97], v[54:57], v[46:49]
	ds_read_b128 v[82:85], v3 offset:128
	ds_read_b128 v[86:89], v3 offset:4480
	ds_read_b128 v[90:93], v3 offset:8832
	ds_read_b128 v[94:97], v3 offset:13184
	s_waitcnt vmcnt(4)
	s_waitcnt lgkmcnt(4)
	v_mfma_f32_16x16x32_f16 v[10:13], v[98:101], v[58:61], v[10:13]
	v_mfma_f32_16x16x32_f16 v[18:21], v[102:105], v[58:61], v[18:21]
	v_mfma_f32_16x16x32_f16 v[26:29], v[106:109], v[58:61], v[26:29]
	v_mfma_f32_16x16x32_f16 v[34:37], v[110:113], v[58:61], v[34:37]
	v_mfma_f32_16x16x32_f16 v[14:17], v[98:101], v[62:65], v[14:17]
	v_mfma_f32_16x16x32_f16 v[22:25], v[102:105], v[62:65], v[22:25]
	v_mfma_f32_16x16x32_f16 v[30:33], v[106:109], v[62:65], v[30:33]
	v_mfma_f32_16x16x32_f16 v[38:41], v[110:113], v[62:65], v[38:41]
	ds_read_b128 v[98:101], v3 offset:192
	ds_read_b128 v[102:105], v3 offset:4544
	ds_read_b128 v[106:109], v3 offset:8896
	ds_read_b128 v[110:113], v3 offset:13248
	s_waitcnt vmcnt(2)
	s_waitcnt lgkmcnt(4)
	v_mfma_f32_16x16x32_f16 v[10:13], v[82:85], v[66:69], v[10:13]
	v_mfma_f32_16x16x32_f16 v[18:21], v[86:89], v[66:69], v[18:21]
	v_mfma_f32_16x16x32_f16 v[26:29], v[90:93], v[66:69], v[26:29]
	v_mfma_f32_16x16x32_f16 v[34:37], v[94:97], v[66:69], v[34:37]
	v_mfma_f32_16x16x32_f16 v[14:17], v[82:85], v[70:73], v[14:17]
	v_mfma_f32_16x16x32_f16 v[22:25], v[86:89], v[70:73], v[22:25]
	v_mfma_f32_16x16x32_f16 v[30:33], v[90:93], v[70:73], v[30:33]
	v_mfma_f32_16x16x32_f16 v[38:41], v[94:97], v[70:73], v[38:41]
	s_waitcnt vmcnt(0)
	s_waitcnt lgkmcnt(0)
	v_mfma_f32_16x16x32_f16 v[10:13], v[98:101], v[74:77], v[10:13]
	v_mfma_f32_16x16x32_f16 v[18:21], v[102:105], v[74:77], v[18:21]
	v_mfma_f32_16x16x32_f16 v[26:29], v[106:109], v[74:77], v[26:29]
	v_mfma_f32_16x16x32_f16 v[34:37], v[110:113], v[74:77], v[34:37]
	v_mfma_f32_16x16x32_f16 v[14:17], v[98:101], v[78:81], v[14:17]
	v_mfma_f32_16x16x32_f16 v[22:25], v[102:105], v[78:81], v[22:25]
	v_mfma_f32_16x16x32_f16 v[30:33], v[106:109], v[78:81], v[30:33]
	v_mfma_f32_16x16x32_f16 v[38:41], v[110:113], v[78:81], v[38:41]
	s_barrier
	v_and_b32_e32 v9, 63, v1
	v_xor_b32_e32 v42, 32, v9
	v_xor_b32_e32 v9, 16, v9
	v_lshlrev_b32_e32 v9, 2, v9
	v_lshlrev_b32_e32 v42, 2, v42
	s_nop 3
	v_max_f32_e32 v10, 0, v10
	v_max_f32_e32 v11, 0, v11
	v_max_f32_e32 v12, 0, v12
	v_max_f32_e32 v13, 0, v13
	v_mov_b32_e32 v2, v10
	v_mul_f32_e32 v3, v10, v10
	v_add_f32_e32 v2, v2, v11
	v_fmac_f32_e32 v3, v11, v11
	v_add_f32_e32 v2, v2, v12
	v_fmac_f32_e32 v3, v12, v12
	v_add_f32_e32 v2, v2, v13
	v_fmac_f32_e32 v3, v13, v13
	v_cvt_pk_f16_f32 v10, v10, v11
	ds_write_b16 v4, v10 offset:0
	ds_write_b16_d16_hi v4, v10 offset:272
	v_cvt_pk_f16_f32 v12, v12, v13
	ds_write_b16 v4, v12 offset:544
	ds_write_b16_d16_hi v4, v12 offset:816
	v_max_f32_e32 v18, 0, v18
	v_max_f32_e32 v19, 0, v19
	v_max_f32_e32 v20, 0, v20
	v_max_f32_e32 v21, 0, v21
	v_add_f32_e32 v2, v2, v18
	v_fmac_f32_e32 v3, v18, v18
	v_add_f32_e32 v2, v2, v19
	v_fmac_f32_e32 v3, v19, v19
	v_add_f32_e32 v2, v2, v20
	v_fmac_f32_e32 v3, v20, v20
	v_add_f32_e32 v2, v2, v21
	v_fmac_f32_e32 v3, v21, v21
	v_cvt_pk_f16_f32 v18, v18, v19
	ds_write_b16 v4, v18 offset:4352
	ds_write_b16_d16_hi v4, v18 offset:4624
	v_cvt_pk_f16_f32 v20, v20, v21
	ds_write_b16 v4, v20 offset:4896
	ds_write_b16_d16_hi v4, v20 offset:5168
	v_max_f32_e32 v26, 0, v26
	v_max_f32_e32 v27, 0, v27
	v_max_f32_e32 v28, 0, v28
	v_max_f32_e32 v29, 0, v29
	v_add_f32_e32 v2, v2, v26
	v_fmac_f32_e32 v3, v26, v26
	v_add_f32_e32 v2, v2, v27
	v_fmac_f32_e32 v3, v27, v27
	v_add_f32_e32 v2, v2, v28
	v_fmac_f32_e32 v3, v28, v28
	v_add_f32_e32 v2, v2, v29
	v_fmac_f32_e32 v3, v29, v29
	v_cvt_pk_f16_f32 v26, v26, v27
	ds_write_b16 v4, v26 offset:8704
	ds_write_b16_d16_hi v4, v26 offset:8976
	v_cvt_pk_f16_f32 v28, v28, v29
	ds_write_b16 v4, v28 offset:9248
	ds_write_b16_d16_hi v4, v28 offset:9520
	v_max_f32_e32 v34, 0, v34
	v_max_f32_e32 v35, 0, v35
	v_max_f32_e32 v36, 0, v36
	v_max_f32_e32 v37, 0, v37
	v_add_f32_e32 v2, v2, v34
	v_fmac_f32_e32 v3, v34, v34
	v_add_f32_e32 v2, v2, v35
	v_fmac_f32_e32 v3, v35, v35
	v_add_f32_e32 v2, v2, v36
	v_fmac_f32_e32 v3, v36, v36
	v_add_f32_e32 v2, v2, v37
	v_fmac_f32_e32 v3, v37, v37
	v_cvt_pk_f16_f32 v34, v34, v35
	ds_write_b16 v4, v34 offset:13056
	ds_write_b16_d16_hi v4, v34 offset:13328
	v_cvt_pk_f16_f32 v36, v36, v37
	ds_write_b16 v4, v36 offset:13600
	ds_write_b16_d16_hi v4, v36 offset:13872
	v_max_f32_e32 v14, 0, v14
	v_max_f32_e32 v15, 0, v15
	v_max_f32_e32 v16, 0, v16
	v_max_f32_e32 v17, 0, v17
	v_mov_b32_e32 v5, v14
	v_mul_f32_e32 v6, v14, v14
	v_add_f32_e32 v5, v5, v15
	v_fmac_f32_e32 v6, v15, v15
	v_add_f32_e32 v5, v5, v16
	v_fmac_f32_e32 v6, v16, v16
	v_add_f32_e32 v5, v5, v17
	v_fmac_f32_e32 v6, v17, v17
	v_cvt_pk_f16_f32 v14, v14, v15
	ds_write_b16 v4, v14 offset:32
	ds_write_b16_d16_hi v4, v14 offset:304
	v_cvt_pk_f16_f32 v16, v16, v17
	ds_write_b16 v4, v16 offset:576
	ds_write_b16_d16_hi v4, v16 offset:848
	v_max_f32_e32 v22, 0, v22
	v_max_f32_e32 v23, 0, v23
	v_max_f32_e32 v24, 0, v24
	v_max_f32_e32 v25, 0, v25
	v_add_f32_e32 v5, v5, v22
	v_fmac_f32_e32 v6, v22, v22
	v_add_f32_e32 v5, v5, v23
	v_fmac_f32_e32 v6, v23, v23
	v_add_f32_e32 v5, v5, v24
	v_fmac_f32_e32 v6, v24, v24
	v_add_f32_e32 v5, v5, v25
	v_fmac_f32_e32 v6, v25, v25
	v_cvt_pk_f16_f32 v22, v22, v23
	ds_write_b16 v4, v22 offset:4384
	ds_write_b16_d16_hi v4, v22 offset:4656
	v_cvt_pk_f16_f32 v24, v24, v25
	ds_write_b16 v4, v24 offset:4928
	ds_write_b16_d16_hi v4, v24 offset:5200
	v_max_f32_e32 v30, 0, v30
	v_max_f32_e32 v31, 0, v31
	v_max_f32_e32 v32, 0, v32
	v_max_f32_e32 v33, 0, v33
	v_add_f32_e32 v5, v5, v30
	v_fmac_f32_e32 v6, v30, v30
	v_add_f32_e32 v5, v5, v31
	v_fmac_f32_e32 v6, v31, v31
	v_add_f32_e32 v5, v5, v32
	v_fmac_f32_e32 v6, v32, v32
	v_add_f32_e32 v5, v5, v33
	v_fmac_f32_e32 v6, v33, v33
	v_cvt_pk_f16_f32 v30, v30, v31
	ds_write_b16 v4, v30 offset:8736
	ds_write_b16_d16_hi v4, v30 offset:9008
	v_cvt_pk_f16_f32 v32, v32, v33
	ds_write_b16 v4, v32 offset:9280
	ds_write_b16_d16_hi v4, v32 offset:9552
	v_max_f32_e32 v38, 0, v38
	v_max_f32_e32 v39, 0, v39
	v_max_f32_e32 v40, 0, v40
	v_max_f32_e32 v41, 0, v41
	v_add_f32_e32 v5, v5, v38
	v_fmac_f32_e32 v6, v38, v38
	v_add_f32_e32 v5, v5, v39
	v_fmac_f32_e32 v6, v39, v39
	v_add_f32_e32 v5, v5, v40
	v_fmac_f32_e32 v6, v40, v40
	v_add_f32_e32 v5, v5, v41
	v_fmac_f32_e32 v6, v41, v41
	v_cvt_pk_f16_f32 v38, v38, v39
	ds_write_b16 v4, v38 offset:13088
	ds_write_b16_d16_hi v4, v38 offset:13360
	v_cvt_pk_f16_f32 v40, v40, v41
	ds_write_b16 v4, v40 offset:13632
	ds_write_b16_d16_hi v4, v40 offset:13904
	ds_bpermute_b32 v11, v9, v2
	ds_bpermute_b32 v13, v9, v3
	ds_bpermute_b32 v15, v9, v5
	ds_bpermute_b32 v17, v9, v6
	s_waitcnt lgkmcnt(0)
	v_add_f32_e32 v2, v2, v11
	v_add_f32_e32 v3, v3, v13
	v_add_f32_e32 v5, v5, v15
	v_add_f32_e32 v6, v6, v17
	ds_bpermute_b32 v11, v42, v2
	ds_bpermute_b32 v13, v42, v3
	ds_bpermute_b32 v15, v42, v5
	ds_bpermute_b32 v17, v42, v6
	s_waitcnt lgkmcnt(0)
	v_add_f32_e32 v2, v2, v11
	v_add_f32_e32 v3, v3, v13
	v_add_f32_e32 v5, v5, v15
	v_add_f32_e32 v6, v6, v17
	v_and_b32_e32 v7, 63, v1
	v_cmp_gt_u32_e32 vcc, 16, v7
	v_lshlrev_b32_e32 v7, 2, v8
	s_and_saveexec_b64 s[42:43], vcc
	ds_write_b32 v7, v2 offset:17408
	ds_write_b32 v7, v3 offset:17920
	ds_write_b32 v7, v5 offset:17472
	ds_write_b32 v7, v6 offset:17984
	s_or_b64 exec, exec, s[42:43]
	s_waitcnt lgkmcnt(0)
	s_barrier
	v_lshrrev_b32_e32 v7, 4, v1
	v_mul_u32_u24_e32 v7, 0x110, v7
	v_and_b32_e32 v9, 15, v1
	v_lshl_add_u32 v7, v9, 4, v7
	ds_read_b128 v[18:21], v7 offset:0
	ds_read_b128 v[22:25], v7 offset:4352
	ds_read_b128 v[26:29], v7 offset:8704
	ds_read_b128 v[30:33], v7 offset:13056
	v_lshlrev_b32_e32 v42, 2, v1
	ds_read_b32 v2, v42 offset:17408
	s_lshl_b32 s40, s3, 8
	s_add_u32 s44, s24, s40
	s_addc_u32 s45, s25, 0
	v_lshlrev_b32_e32 v9, 4, v1
	s_waitcnt lgkmcnt(4)
	global_store_dwordx4 v9, v[18:21], s[44:45] nt
	v_add_u32_e32 v9, 0x1000, v9
	s_waitcnt lgkmcnt(3)
	global_store_dwordx4 v9, v[22:25], s[44:45] nt
	v_add_u32_e32 v9, 0x1000, v9
	s_waitcnt lgkmcnt(2)
	global_store_dwordx4 v9, v[26:29], s[44:45] nt
	v_add_u32_e32 v9, 0x1000, v9
	s_waitcnt lgkmcnt(1)
	global_store_dwordx4 v9, v[30:33], s[44:45] nt
	s_lshl_b32 s40, s2, 8
	s_and_b32 s40, s40, 0xf00
	v_add_lshl_u32 v42, s40, v1, 2
	s_waitcnt lgkmcnt(0)
	global_atomic_add_f32 v42, v2, s[8:9]
	s_endpgm

amdhsa.kernels:
  - .agpr_count:     0
    .args:
      - .actual_access:  read_only
        .address_space:  global
        .offset:         0
        .size:           8
        .value_kind:     global_buffer
      - .actual_access:  read_only
        .address_space:  global
        .offset:         8
        .size:           8
        .value_kind:     global_buffer
      - .actual_access:  read_only
        .address_space:  global
        .offset:         16
        .size:           8
        .value_kind:     global_buffer
      - .actual_access:  read_only
        .address_space:  global
        .offset:         24
        .size:           8
        .value_kind:     global_buffer
      - .actual_access:  write_only
        .address_space:  global
        .offset:         32
        .size:           8
        .value_kind:     global_buffer
      - .actual_access:  write_only
        .address_space:  global
        .offset:         40
        .size:           8
        .value_kind:     global_buffer
    .group_segment_fixed_size: 56512
    .kernarg_segment_align: 8
    .kernarg_segment_size: 48
    .language:       OpenCL C
    .language_version:
      - 2
      - 0
    .max_flat_workgroup_size: 1024
    .name:           _Z10k_bscatterPKiS0_PKfS0_PiP15HIP_vector_typeIiLj2EE
    .private_segment_fixed_size: 0
    .sgpr_count:     42
    .sgpr_spill_count: 0
    .symbol:         _Z10k_bscatterPKiS0_PKfS0_PiP15HIP_vector_typeIiLj2EE.kd
    .uniform_work_group_size: 1
    .uses_dynamic_stack: false
    .vgpr_count:     89
    .vgpr_spill_count: 0
    .wavefront_size: 64
  - .agpr_count:     0
    .args:
      - .actual_access:  read_only
        .address_space:  global
        .offset:         0
        .size:           8
        .value_kind:     global_buffer
      - .actual_access:  read_only
        .address_space:  global
        .offset:         8
        .size:           8
        .value_kind:     global_buffer
      - .actual_access:  write_only
        .address_space:  global
        .offset:         16
        .size:           8
        .value_kind:     global_buffer
      - .actual_access:  write_only
        .address_space:  global
        .offset:         24
        .size:           8
        .value_kind:     global_buffer
      - .actual_access:  write_only
        .address_space:  global
        .offset:         32
        .size:           8
        .value_kind:     global_buffer
      - .actual_access:  write_only
        .address_space:  global
        .offset:         40
        .size:           8
        .value_kind:     global_buffer
      - .actual_access:  read_only
        .address_space:  global
        .offset:         48
        .size:           8
        .value_kind:     global_buffer
      - .actual_access:  write_only
        .address_space:  global
        .offset:         56
        .size:           8
        .value_kind:     global_buffer
    .group_segment_fixed_size: 12352
    .kernarg_segment_align: 8
    .kernarg_segment_size: 64
    .language:       OpenCL C
    .language_version:
      - 2
      - 0
    .max_flat_workgroup_size: 1024
    .name:           _Z8k_bfinalPK15HIP_vector_typeIiLj2EEPKiPS0_PiS6_PfPKfPDF16_
    .private_segment_fixed_size: 0
    .sgpr_count:     38
    .sgpr_spill_count: 0
    .symbol:         _Z8k_bfinalPK15HIP_vector_typeIiLj2EEPKiPS0_PiS6_PfPKfPDF16_.kd
    .uniform_work_group_size: 1
    .uses_dynamic_stack: false
    .vgpr_count:     72
    .vgpr_spill_count: 0
    .wavefront_size: 64
  - .agpr_count:     0
    .args:
      - .actual_access:  read_only
        .address_space:  global
        .offset:         0
        .size:           8
        .value_kind:     global_buffer
      - .actual_access:  write_only
        .address_space:  global
        .offset:         8
        .size:           8
        .value_kind:     global_buffer
      - .actual_access:  write_only
        .address_space:  global
        .offset:         16
        .size:           8
        .value_kind:     global_buffer
      - .actual_access:  read_only
        .address_space:  global
        .offset:         24
        .size:           8
        .value_kind:     global_buffer
      - .actual_access:  read_only
        .address_space:  global
        .offset:         32
        .size:           8
        .value_kind:     global_buffer
      - .actual_access:  write_only
        .address_space:  global
        .offset:         40
        .size:           8
        .value_kind:     global_buffer
      - .actual_access:  read_only
        .address_space:  global
        .offset:         48
        .size:           8
        .value_kind:     global_buffer
      - .actual_access:  read_only
        .address_space:  global
        .offset:         56
        .size:           8
        .value_kind:     global_buffer
      - .actual_access:  read_only
        .address_space:  global
        .offset:         64
        .size:           8
        .value_kind:     global_buffer
      - .actual_access:  read_only
        .address_space:  global
        .offset:         72
        .size:           8
        .value_kind:     global_buffer
      - .actual_access:  read_only
        .address_space:  global
        .offset:         80
        .size:           8
        .value_kind:     global_buffer
      - .actual_access:  read_only
        .address_space:  global
        .offset:         88
        .size:           8
        .value_kind:     global_buffer
      - .actual_access:  write_only
        .address_space:  global
        .offset:         96
        .size:           8
        .value_kind:     global_buffer
      - .actual_access:  write_only
        .address_space:  global
        .offset:         104
        .size:           8
        .value_kind:     global_buffer
      - .actual_access:  write_only
        .address_space:  global
        .offset:         112
        .size:           8
        .value_kind:     global_buffer
      - .actual_access:  write_only
        .address_space:  global
        .offset:         120
        .size:           8
        .value_kind:     global_buffer
      - .actual_access:  write_only
        .address_space:  global
        .offset:         128
        .size:           8
        .value_kind:     global_buffer
    .group_segment_fixed_size: 628
    .kernarg_segment_align: 8
    .kernarg_segment_size: 136
    .language:       OpenCL C
    .language_version:
      - 2
      - 0
    .max_flat_workgroup_size: 1024
    .name:           _Z7k_bhistPKiPiPfPKfS4_PDF16_S4_S4_S4_S4_S4_S4_S5_S5_S5_S5_S2_
    .private_segment_fixed_size: 0
    .sgpr_count:     25
    .sgpr_spill_count: 0
    .symbol:         _Z7k_bhistPKiPiPfPKfS4_PDF16_S4_S4_S4_S4_S4_S4_S5_S5_S5_S5_S2_.kd
    .uniform_work_group_size: 1
    .uses_dynamic_stack: false
    .vgpr_count:     32
    .vgpr_spill_count: 0
    .wavefront_size: 64
  - .agpr_count:     0
    .args:
      - .actual_access:  read_only
        .address_space:  global
        .offset:         0
        .size:           8
        .value_kind:     global_buffer
      - .actual_access:  read_only
        .address_space:  global
        .offset:         8
        .size:           8
        .value_kind:     global_buffer
      - .actual_access:  read_only
        .address_space:  global
        .offset:         16
        .size:           8
        .value_kind:     global_buffer
      - .actual_access:  read_only
        .address_space:  global
        .offset:         24
        .size:           8
        .value_kind:     global_buffer
      - .actual_access:  read_only
        .address_space:  global
        .offset:         32
        .size:           8
        .value_kind:     global_buffer
      - .actual_access:  read_only
        .address_space:  global
        .offset:         40
        .size:           8
        .value_kind:     global_buffer
      - .actual_access:  read_only
        .address_space:  global
        .offset:         48
        .size:           8
        .value_kind:     global_buffer
      - .actual_access:  read_only
        .address_space:  global
        .offset:         56
        .size:           8
        .value_kind:     global_buffer
      - .actual_access:  read_only
        .address_space:  global
        .offset:         64
        .size:           8
        .value_kind:     global_buffer
      - .actual_access:  write_only
        .address_space:  global
        .offset:         72
        .size:           8
        .value_kind:     global_buffer
      - .actual_access:  write_only
        .address_space:  global
        .offset:         80
        .size:           8
        .value_kind:     global_buffer
      - .offset:         88
        .size:           4
        .value_kind:     hidden_block_count_x
      - .offset:         92
        .size:           4
        .value_kind:     hidden_block_count_y
      - .offset:         96
        .size:           4
        .value_kind:     hidden_block_count_z
      - .offset:         100
        .size:           2
        .value_kind:     hidden_group_size_x
      - .offset:         102
        .size:           2
        .value_kind:     hidden_group_size_y
      - .offset:         104
        .size:           2
        .value_kind:     hidden_group_size_z
      - .offset:         106
        .size:           2
        .value_kind:     hidden_remainder_x
      - .offset:         108
        .size:           2
        .value_kind:     hidden_remainder_y
      - .offset:         110
        .size:           2
        .value_kind:     hidden_remainder_z
      - .offset:         128
        .size:           8
        .value_kind:     hidden_global_offset_x
      - .offset:         136
        .size:           8
        .value_kind:     hidden_global_offset_y
      - .offset:         144
        .size:           8
        .value_kind:     hidden_global_offset_z
      - .offset:         152
        .size:           2
        .value_kind:     hidden_grid_dims
    .group_segment_fixed_size: 2048
    .kernarg_segment_align: 8
    .kernarg_segment_size: 344
    .language:       OpenCL C
    .language_version:
      - 2
      - 0
    .max_flat_workgroup_size: 256
    .name:           _Z7k_fold2PKfS0_S0_S0_S0_S0_S0_S0_S0_PDF16_Pf
    .private_segment_fixed_size: 0
    .sgpr_count:     36
    .sgpr_spill_count: 0
    .symbol:         _Z7k_fold2PKfS0_S0_S0_S0_S0_S0_S0_S0_PDF16_Pf.kd
    .uniform_work_group_size: 1
    .uses_dynamic_stack: false
    .vgpr_count:     61
    .vgpr_spill_count: 0
    .wavefront_size: 64
  - .agpr_count:     0
    .args:
      - .actual_access:  read_only
        .address_space:  global
        .offset:         0
        .size:           8
        .value_kind:     global_buffer
      - .actual_access:  read_only
        .address_space:  global
        .offset:         8
        .size:           8
        .value_kind:     global_buffer
      - .actual_access:  write_only
        .address_space:  global
        .offset:         16
        .size:           8
        .value_kind:     global_buffer
      - .actual_access:  read_only
        .address_space:  global
        .offset:         24
        .size:           8
        .value_kind:     global_buffer
      - .actual_access:  read_only
        .address_space:  global
        .offset:         32
        .size:           8
        .value_kind:     global_buffer
      - .actual_access:  read_only
        .address_space:  global
        .offset:         40
        .size:           8
        .value_kind:     global_buffer
      - .actual_access:  read_only
        .address_space:  global
        .offset:         48
        .size:           8
        .value_kind:     global_buffer
      - .actual_access:  read_only
        .address_space:  global
        .offset:         56
        .size:           8
        .value_kind:     global_buffer
      - .actual_access:  read_only
        .address_space:  global
        .offset:         64
        .size:           8
        .value_kind:     global_buffer
      - .actual_access:  read_only
        .address_space:  global
        .offset:         72
        .size:           8
        .value_kind:     global_buffer
      - .actual_access:  read_only
        .address_space:  global
        .offset:         80
        .size:           8
        .value_kind:     global_buffer
      - .actual_access:  write_only
        .address_space:  global
        .offset:         88
        .size:           8
        .value_kind:     global_buffer
      - .actual_access:  write_only
        .address_space:  global
        .offset:         96
        .size:           8
        .value_kind:     global_buffer
      - .address_space:  global
        .offset:         104
        .size:           8
        .value_kind:     global_buffer
      - .actual_access:  write_only
        .address_space:  global
        .offset:         112
        .size:           8
        .value_kind:     global_buffer
      - .actual_access:  read_only
        .address_space:  global
        .offset:         120
        .size:           8
        .value_kind:     global_buffer
      - .actual_access:  read_only
        .address_space:  global
        .offset:         128
        .size:           8
        .value_kind:     global_buffer
    .group_segment_fixed_size: 22272
    .kernarg_segment_align: 8
    .kernarg_segment_size: 136
    .language:       OpenCL C
    .language_version:
      - 2
      - 0
    .max_flat_workgroup_size: 256
    .name:           _Z5k_gcnILi1EEvPKvPK15HIP_vector_typeIiLj2EEPfPKiS8_PKfPKDF16_SA_SA_SA_SA_S6_PDF16_S6_SD_SC_SA_
    .private_segment_fixed_size: 0
    .sgpr_count:     35
    .sgpr_spill_count: 0
    .symbol:         _Z5k_gcnILi1EEvPKvPK15HIP_vector_typeIiLj2EEPfPKiS8_PKfPKDF16_SA_SA_SA_SA_S6_PDF16_S6_SD_SC_SA_.kd
    .uniform_work_group_size: 1
    .uses_dynamic_stack: false
    .vgpr_count:     72
    .vgpr_spill_count: 0
    .wavefront_size: 64
  - .agpr_count:     0
    .args:
      - .actual_access:  read_only
        .address_space:  global
        .offset:         0
        .size:           8
        .value_kind:     global_buffer
      - .actual_access:  read_only
        .address_space:  global
        .offset:         8
        .size:           8
        .value_kind:     global_buffer
      - .actual_access:  read_only
        .address_space:  global
        .offset:         16
        .size:           8
        .value_kind:     global_buffer
      - .actual_access:  read_only
        .address_space:  global
        .offset:         24
        .size:           8
        .value_kind:     global_buffer
      - .actual_access:  read_only
        .address_space:  global
        .offset:         32
        .size:           8
        .value_kind:     global_buffer
      - .actual_access:  read_only
        .address_space:  global
        .offset:         40
        .size:           8
        .value_kind:     global_buffer
      - .actual_access:  read_only
        .address_space:  global
        .offset:         48
        .size:           8
        .value_kind:     global_buffer
      - .actual_access:  read_only
        .address_space:  global
        .offset:         56
        .size:           8
        .value_kind:     global_buffer
      - .actual_access:  read_only
        .address_space:  global
        .offset:         64
        .size:           8
        .value_kind:     global_buffer
      - .actual_access:  read_only
        .address_space:  global
        .offset:         72
        .size:           8
        .value_kind:     global_buffer
      - .actual_access:  read_only
        .address_space:  global
        .offset:         80
        .size:           8
        .value_kind:     global_buffer
      - .actual_access:  read_only
        .address_space:  global
        .offset:         88
        .size:           8
        .value_kind:     global_buffer
      - .actual_access:  write_only
        .address_space:  global
        .offset:         96
        .size:           8
        .value_kind:     global_buffer
      - .address_space:  global
        .offset:         104
        .size:           8
        .value_kind:     global_buffer
      - .actual_access:  read_only
        .address_space:  global
        .offset:         112
        .size:           8
        .value_kind:     global_buffer
      - .actual_access:  read_only
        .address_space:  global
        .offset:         120
        .size:           8
        .value_kind:     global_buffer
      - .actual_access:  read_only
        .address_space:  global
        .offset:         128
        .size:           8
        .value_kind:     global_buffer
      - .offset:         136
        .size:           4
        .value_kind:     hidden_block_count_x
      - .offset:         140
        .size:           4
        .value_kind:     hidden_block_count_y
      - .offset:         144
        .size:           4
        .value_kind:     hidden_block_count_z
      - .offset:         148
        .size:           2
        .value_kind:     hidden_group_size_x
      - .offset:         150
        .size:           2
        .value_kind:     hidden_group_size_y
      - .offset:         152
        .size:           2
        .value_kind:     hidden_group_size_z
      - .offset:         154
        .size:           2
        .value_kind:     hidden_remainder_x
      - .offset:         156
        .size:           2
        .value_kind:     hidden_remainder_y
      - .offset:         158
        .size:           2
        .value_kind:     hidden_remainder_z
      - .offset:         176
        .size:           8
        .value_kind:     hidden_global_offset_x
      - .offset:         184
        .size:           8
        .value_kind:     hidden_global_offset_y
      - .offset:         192
        .size:           8
        .value_kind:     hidden_global_offset_z
      - .offset:         200
        .size:           2
        .value_kind:     hidden_grid_dims
    .group_segment_fixed_size: 23808
    .kernarg_segment_align: 8
    .kernarg_segment_size: 392
    .language:       OpenCL C
    .language_version:
      - 2
      - 0
    .max_flat_workgroup_size: 256
    .name:           _Z5k_gcnILi2EEvPKvPK15HIP_vector_typeIiLj2EEPfPKiS8_PKfPKDF16_SA_SA_SA_SA_S6_PDF16_S6_SD_SC_SA_
    .private_segment_fixed_size: 0
    .sgpr_count:     36
    .sgpr_spill_count: 0
    .symbol:         _Z5k_gcnILi2EEvPKvPK15HIP_vector_typeIiLj2EEPfPKiS8_PKfPKDF16_SA_SA_SA_SA_S6_PDF16_S6_SD_SC_SA_.kd
    .uniform_work_group_size: 1
    .uses_dynamic_stack: false
    .vgpr_count:     128
    .vgpr_spill_count: 0
    .wavefront_size: 64
  - .agpr_count:     0
    .args:
      - .actual_access:  read_only
        .address_space:  global
        .offset:         0
        .size:           8
        .value_kind:     global_buffer
      - .actual_access:  read_only
        .address_space:  global
        .offset:         8
        .size:           8
        .value_kind:     global_buffer
      - .actual_access:  read_only
        .address_space:  global
        .offset:         16
        .size:           8
        .value_kind:     global_buffer
      - .actual_access:  read_only
        .address_space:  global
        .offset:         24
        .size:           8
        .value_kind:     global_buffer
      - .actual_access:  write_only
        .address_space:  global
        .offset:         32
        .size:           8
        .value_kind:     global_buffer
      - .actual_access:  read_only
        .address_space:  global
        .offset:         40
        .size:           8
        .value_kind:     global_buffer
      - .actual_access:  read_only
        .address_space:  global
        .offset:         48
        .size:           8
        .value_kind:     global_buffer
      - .actual_access:  read_only
        .address_space:  global
        .offset:         56
        .size:           8
        .value_kind:     global_buffer
      - .actual_access:  read_only
        .address_space:  global
        .offset:         64
        .size:           8
        .value_kind:     global_buffer
      - .actual_access:  read_only
        .address_space:  global
        .offset:         72
        .size:           8
        .value_kind:     global_buffer
      - .actual_access:  read_only
        .address_space:  global
        .offset:         80
        .size:           8
        .value_kind:     global_buffer
      - .actual_access:  read_only
        .address_space:  global
        .offset:         88
        .size:           8
        .value_kind:     global_buffer
      - .actual_access:  write_only
        .address_space:  global
        .offset:         96
        .size:           8
        .value_kind:     global_buffer
    .group_segment_fixed_size: 9216
    .kernarg_segment_align: 8
    .kernarg_segment_size: 104
    .language:       OpenCL C
    .language_version:
      - 2
      - 0
    .max_flat_workgroup_size: 512
    .name:           _Z6k_lstmILi256ELi10ELb1ELb0EEvPKDF16_S1_S1_PKfPDF16_S1_S1_S1_S3_S3_S3_PfS5_
    .private_segment_fixed_size: 0
    .sgpr_count:     37
    .sgpr_spill_count: 0
    .symbol:         _Z6k_lstmILi256ELi10ELb1ELb0EEvPKDF16_S1_S1_PKfPDF16_S1_S1_S1_S3_S3_S3_PfS5_.kd
    .uniform_work_group_size: 1
    .uses_dynamic_stack: false
    .vgpr_count:     256
    .vgpr_spill_count: 0
    .wavefront_size: 64
  - .agpr_count:     0
    .args:
      - .actual_access:  read_only
        .address_space:  global
        .offset:         0
        .size:           8
        .value_kind:     global_buffer
      - .actual_access:  read_only
        .address_space:  global
        .offset:         8
        .size:           8
        .value_kind:     global_buffer
      - .actual_access:  read_only
        .address_space:  global
        .offset:         16
        .size:           8
        .value_kind:     global_buffer
      - .actual_access:  read_only
        .address_space:  global
        .offset:         24
        .size:           8
        .value_kind:     global_buffer
      - .actual_access:  read_only
        .address_space:  global
        .offset:         32
        .size:           8
        .value_kind:     global_buffer
      - .actual_access:  read_only
        .address_space:  global
        .offset:         40
        .size:           8
        .value_kind:     global_buffer
      - .actual_access:  read_only
        .address_space:  global
        .offset:         48
        .size:           8
        .value_kind:     global_buffer
      - .actual_access:  read_only
        .address_space:  global
        .offset:         56
        .size:           8
        .value_kind:     global_buffer
      - .actual_access:  read_only
        .address_space:  global
        .offset:         64
        .size:           8
        .value_kind:     global_buffer
      - .actual_access:  read_only
        .address_space:  global
        .offset:         72
        .size:           8
        .value_kind:     global_buffer
      - .actual_access:  read_only
        .address_space:  global
        .offset:         80
        .size:           8
        .value_kind:     global_buffer
      - .actual_access:  write_only
        .address_space:  global
        .offset:         88
        .size:           8
        .value_kind:     global_buffer
      - .actual_access:  read_only
        .address_space:  global
        .offset:         96
        .size:           8
        .value_kind:     global_buffer
    .group_segment_fixed_size: 0
    .kernarg_segment_align: 8
    .kernarg_segment_size: 104
    .language:       OpenCL C
    .language_version:
      - 2
      - 0
    .max_flat_workgroup_size: 512
    .name:           _Z6k_lstmILi128ELi8ELb0ELb1EEvPKDF16_S1_S1_PKfPDF16_S1_S1_S1_S3_S3_S3_PfS5_
    .private_segment_fixed_size: 0
    .sgpr_count:     46
    .sgpr_spill_count: 0
    .symbol:         _Z6k_lstmILi128ELi8ELb0ELb1EEvPKDF16_S1_S1_PKfPDF16_S1_S1_S1_S3_S3_S3_PfS5_.kd
    .uniform_work_group_size: 1
    .uses_dynamic_stack: false
    .vgpr_count:     256
    .vgpr_spill_count: 0
    .wavefront_size: 64
